# P7 K-loop LDS-DMA staging rebalanced 2/6/2/6 -> 4/4/4/4 per load segment (Bs half staged one segment later)
# speedup vs baseline: 1.0011x; 1.0011x over previous
.LBB0_973:
	v_readlane_b32 s68, v239, 42
	s_lshl_b32 s24, s18, 6
	s_lshl_b32 s25, s18, 13
	s_lshl_b32 s18, s4, 5
	v_readlane_b32 s69, v239, 43
	s_and_b32 s26, s18, 0x60
	v_readlane_b32 s70, v239, 44
	v_readlane_b32 s71, v239, 45
	v_readlane_b32 s72, v239, 46
	v_readlane_b32 s73, v239, 47
	s_mov_b64 s[44:45], s[68:69]
	s_lshr_b32 s27, s26, 3
	s_mov_b64 s[46:47], s[70:71]
	s_add_u32 s18, s46, 0x16000080
	s_mov_b64 s[20:21], 0x80
	s_addc_u32 s19, s47, 0
	s_add_i32 m0, s35, 0x18000
	v_lshl_add_u64 v[6:7], v[6:7], 0, s[20:21]
	s_mov_b64 s[48:49], s[72:73]
	s_waitcnt vmcnt(2)
	s_barrier
	global_load_lds_dwordx4 v[6:7], off
	v_lshl_add_u64 v[4:5], v[4:5], 0, s[20:21]
	s_add_i32 m0, s35, 0x1a000
	s_add_i32 s68, s35, 0x8000
	s_add_i32 s69, s35, 0xa000
	global_load_lds_dwordx4 v[4:5], off
	v_lshl_add_u64 v[4:5], s[18:19], 0, v[198:199]
	s_mov_b32 m0, s68
	s_add_u32 s22, s38, 0x20080
	global_load_lds_dwordx4 v[4:5], off
	v_lshl_add_u64 v[4:5], s[18:19], 0, v[200:201]
	s_mov_b32 m0, s69
	s_addc_u32 s23, s39, 0
	s_mov_b64 s[100:101], s[22:23]
	global_load_lds_dwordx4 v[4:5], off
	s_add_i32 m0, s35, 0x1c000
	v_lshl_add_u64 v[4:5], s[22:23], 0, v[194:195]
	global_load_lds_dwordx4 v[4:5], off
	v_lshl_add_u64 v[4:5], s[22:23], 0, v[196:197]
	s_add_i32 m0, s35, 0x1e000
	s_and_b32 s22, s2, 0xffffffc0
	global_load_lds_dwordx4 v[4:5], off
	v_and_b32_e32 v4, 15, v1
	v_bfe_u32 v3, v1, 5, 1
	v_lshlrev_b32_e32 v6, 1, v1
	s_ashr_i32 s23, s22, 31
	v_and_b32_e32 v6, 32, v6
	v_lshlrev_b32_e32 v7, 6, v4
	v_lshlrev_b32_e32 v10, 10, v3
	v_lshlrev_b32_e32 v11, 2, v1
	v_or_b32_e32 v3, s27, v3
	s_lshl_b64 s[22:23], s[22:23], 2
	v_or_b32_e32 v9, v7, v6
	v_and_b32_e32 v11, 32, v11
	v_lshlrev_b32_e32 v3, 10, v3
	s_add_u32 s22, s5, s22
	v_bitop3_b32 v217, v3, v9, v11 bitop3:0xf6
	s_addc_u32 s23, s11, s23
	v_mov_b32_e32 v3, v199
	s_lshl_b32 s4, s4, 8
	v_lshl_add_u64 v[202:203], s[22:23], 0, v[2:3]
	s_add_i32 s70, s4, 0
	v_bfe_u32 v2, v8, 4, 1
	v_lshrrev_b32_e32 v5, 4, v8
	v_bitop3_b32 v6, v7, v11, v6 bitop3:0x36
	s_waitcnt vmcnt(0)
	s_add_i32 s70, s70, 0x23400
	v_lshlrev_b32_e32 v3, 4, v2
	v_lshlrev_b32_e32 v2, 3, v2
	v_readlane_b32 s74, v239, 48
	v_or3_b32 v6, s25, v10, v6
	s_cmpk_lt_u32 s2, 0x100
	v_sub_co_u32_e32 v204, vcc, 0, v2
	v_or3_b32 v218, v4, v3, s24
	v_lshl_or_b32 v219, v5, 3, s26
	v_add_u32_e32 v2, 0, v217
	s_mov_b32 s24, 0xbd9d265f
	s_mov_b32 s26, 0xbc5083aa
	s_cselect_b64 s[22:23], -1, 0
	v_subb_co_u32_e64 v205, s[4:5], 0, 0, vcc
	v_add_u32_e32 v220, 0x10000, v2
	v_add_u32_e32 v221, 0x14000, v2
	v_add_u32_e32 v222, 0, v6
	s_mov_b32 s25, 0x401d265f
	s_mov_b32 s27, 0x3ed083aa
	s_mov_b32 s71, 0xc05083aa
	v_mov_b32_e32 v223, 0x401c62bf
	s_mov_b32 s74, s28
	s_mov_b32 s72, s1
	v_readlane_b32 s75, v239, 49
	s_barrier
	s_branch .LBB0_976

.LBB0_985:
	s_mov_b32 s88, 0
	s_waitcnt lgkmcnt(0)
	v_mov_b32_e32 v201, v199
	v_lshl_add_u64 v[210:211], s[46:47], 0, v[198:199]
	v_lshl_add_u64 v[212:213], s[46:47], 0, v[200:201]
	s_barrier
	s_setprio 1
	s_waitcnt lgkmcnt(0)
	v_mfma_f32_16x16x128_f8f6f4 v[126:129], v[18:25], v[58:65], v[126:129]
	v_mfma_f32_16x16x128_f8f6f4 v[122:125], v[26:33], v[58:65], v[122:125]
	v_mfma_f32_16x16x128_f8f6f4 v[110:113], v[18:25], v[50:57], v[110:113]
	v_mfma_f32_16x16x128_f8f6f4 v[106:109], v[26:33], v[50:57], v[106:109]
	v_mfma_f32_16x16x128_f8f6f4 v[86:89], v[18:25], v[42:49], v[86:89]
	v_mfma_f32_16x16x128_f8f6f4 v[82:85], v[26:33], v[42:49], v[82:85]
	v_mfma_f32_16x16x128_f8f6f4 v[70:73], v[18:25], v[34:41], v[70:73]
	v_mfma_f32_16x16x128_f8f6f4 v[66:69], v[26:33], v[34:41], v[66:69]
	s_setprio 0
	s_setprio 1
	v_mfma_f32_16x16x128_f8f6f4 v[118:121], v[2:9], v[58:65], v[118:121]
	v_mfma_f32_16x16x128_f8f6f4 v[114:117], v[10:17], v[58:65], v[114:117]
	v_mfma_f32_16x16x128_f8f6f4 v[102:105], v[2:9], v[50:57], v[102:105]
	v_mfma_f32_16x16x128_f8f6f4 v[90:93], v[10:17], v[50:57], v[90:93]
	v_mfma_f32_16x16x128_f8f6f4 v[94:97], v[2:9], v[42:49], v[94:97]
	v_mfma_f32_16x16x128_f8f6f4 v[98:101], v[10:17], v[42:49], v[98:101]
	v_mfma_f32_16x16x128_f8f6f4 v[74:77], v[2:9], v[34:41], v[74:77]
	v_mfma_f32_16x16x128_f8f6f4 v[78:81], v[10:17], v[34:41], v[78:81]
	s_setprio 0
	s_barrier
	s_add_i32 s48, 0, 0x18000
	s_add_i32 s49, 0, 0x1c000
	v_add_u32_e32 v14, s48, v217
	v_add_u32_e32 v30, s49, v217
	ds_read_b128 v[2:5], v14
	ds_read_b128 v[6:9], v14 offset:16
	ds_read_b128 v[10:13], v14 offset:2048
	ds_read_b128 v[14:17], v14 offset:2064
	ds_read_b128 v[18:21], v30
	ds_read_b128 v[22:25], v30 offset:16
	ds_read_b128 v[26:29], v30 offset:2048
	ds_read_b128 v[30:33], v30 offset:2064
	v_lshl_add_u64 v[240:241], s[98:99], 0, v[194:195]
	s_mov_b32 m0, s62
	s_nop 0
	global_load_lds_dwordx4 v[240:241], off
	v_lshl_add_u64 v[240:241], s[98:99], 0, v[196:197]
	s_mov_b32 m0, s63
	s_nop 0
	global_load_lds_dwordx4 v[240:241], off
	s_mov_b32 m0, s65
	ds_read_b128 v[34:37], v222 offset:32768
	ds_read_b128 v[38:41], v222 offset:32784
	ds_read_b128 v[42:45], v222 offset:34816
	ds_read_b128 v[46:49], v222 offset:34832
	ds_read_b128 v[50:53], v222 offset:36864
	ds_read_b128 v[54:57], v222 offset:36880
	ds_read_b128 v[58:61], v222 offset:38912
	ds_read_b128 v[62:65], v222 offset:38928
	global_load_lds_dwordx4 v215, s[46:47]
	s_mov_b32 m0, s66
	s_nop 0
	global_load_lds_dwordx4 v216, s[46:47]
	s_waitcnt vmcnt(8)
	s_waitcnt lgkmcnt(0)
	s_barrier
	s_setprio 1
	s_waitcnt lgkmcnt(0)
	v_mfma_f32_16x16x128_f8f6f4 v[190:193], v[2:9], v[34:41], v[190:193]
	v_mfma_f32_16x16x128_f8f6f4 v[186:189], v[10:17], v[34:41], v[186:189]
	v_mfma_f32_16x16x128_f8f6f4 v[174:177], v[2:9], v[42:49], v[174:177]
	v_mfma_f32_16x16x128_f8f6f4 v[170:173], v[10:17], v[42:49], v[170:173]
	v_mfma_f32_16x16x128_f8f6f4 v[158:161], v[2:9], v[50:57], v[158:161]
	v_mfma_f32_16x16x128_f8f6f4 v[154:157], v[10:17], v[50:57], v[154:157]
	v_mfma_f32_16x16x128_f8f6f4 v[142:145], v[2:9], v[58:65], v[142:145]
	v_mfma_f32_16x16x128_f8f6f4 v[138:141], v[10:17], v[58:65], v[138:141]
	s_setprio 0
	s_setprio 1
	v_mfma_f32_16x16x128_f8f6f4 v[182:185], v[18:25], v[34:41], v[182:185]
	v_mfma_f32_16x16x128_f8f6f4 v[178:181], v[26:33], v[34:41], v[178:181]
	v_mfma_f32_16x16x128_f8f6f4 v[166:169], v[18:25], v[42:49], v[166:169]
	v_mfma_f32_16x16x128_f8f6f4 v[162:165], v[26:33], v[42:49], v[162:165]
	v_mfma_f32_16x16x128_f8f6f4 v[150:153], v[18:25], v[50:57], v[150:153]
	v_mfma_f32_16x16x128_f8f6f4 v[146:149], v[26:33], v[50:57], v[146:149]
	v_mfma_f32_16x16x128_f8f6f4 v[134:137], v[18:25], v[58:65], v[134:137]
	v_mfma_f32_16x16x128_f8f6f4 v[130:133], v[26:33], v[58:65], v[130:133]
	s_setprio 0
	s_barrier
	s_add_i32 s46, s48, s52
	v_lshl_add_u64 v[208:209], v[208:209], 0, s[20:21]
	s_mov_b32 m0, s46
	ds_read_b128 v[34:37], v222 offset:49152
	ds_read_b128 v[38:41], v222 offset:49168
	ds_read_b128 v[42:45], v222 offset:51200
	ds_read_b128 v[46:49], v222 offset:51216
	ds_read_b128 v[50:53], v222 offset:53248
	ds_read_b128 v[54:57], v222 offset:53264
	ds_read_b128 v[58:61], v222 offset:55296
	ds_read_b128 v[62:65], v222 offset:55312
	global_load_lds_dwordx4 v[208:209], off
	s_add_i32 m0, s46, 0x2000
	s_add_u32 s44, s44, 0x20080
	v_lshl_add_u64 v[206:207], v[206:207], 0, s[20:21]
	s_addc_u32 s45, s45, 0
	s_add_i32 s46, s49, s52
	global_load_lds_dwordx4 v[206:207], off
	s_mov_b64 s[100:101], s[44:45]
	v_lshl_add_u64 v[206:207], v[210:211], 0, s[20:21]
	s_mov_b32 m0, s68
	s_nop 0
	global_load_lds_dwordx4 v[206:207], off
	v_lshl_add_u64 v[206:207], v[212:213], 0, s[20:21]
	s_mov_b32 m0, s69
	s_nop 0
	global_load_lds_dwordx4 v[206:207], off
	s_waitcnt vmcnt(6)
	s_waitcnt lgkmcnt(0)
	s_barrier
	s_setprio 1
	s_waitcnt lgkmcnt(0)
	v_mfma_f32_16x16x128_f8f6f4 v[126:129], v[2:9], v[34:41], v[126:129]
	v_mfma_f32_16x16x128_f8f6f4 v[122:125], v[10:17], v[34:41], v[122:125]
	v_mfma_f32_16x16x128_f8f6f4 v[110:113], v[2:9], v[42:49], v[110:113]
	v_mfma_f32_16x16x128_f8f6f4 v[106:109], v[10:17], v[42:49], v[106:109]
	v_mfma_f32_16x16x128_f8f6f4 v[86:89], v[2:9], v[50:57], v[86:89]
	v_mfma_f32_16x16x128_f8f6f4 v[82:85], v[10:17], v[50:57], v[82:85]
	v_mfma_f32_16x16x128_f8f6f4 v[70:73], v[2:9], v[58:65], v[70:73]
	v_mfma_f32_16x16x128_f8f6f4 v[66:69], v[10:17], v[58:65], v[66:69]
	s_setprio 0
	s_setprio 1
	v_mfma_f32_16x16x128_f8f6f4 v[118:121], v[18:25], v[34:41], v[118:121]
	v_mfma_f32_16x16x128_f8f6f4 v[114:117], v[26:33], v[34:41], v[114:117]
	v_mfma_f32_16x16x128_f8f6f4 v[102:105], v[18:25], v[42:49], v[102:105]
	v_mfma_f32_16x16x128_f8f6f4 v[90:93], v[26:33], v[42:49], v[90:93]
	v_mfma_f32_16x16x128_f8f6f4 v[94:97], v[18:25], v[50:57], v[94:97]
	v_mfma_f32_16x16x128_f8f6f4 v[98:101], v[26:33], v[50:57], v[98:101]
	v_mfma_f32_16x16x128_f8f6f4 v[74:77], v[18:25], v[58:65], v[74:77]
	v_mfma_f32_16x16x128_f8f6f4 v[78:81], v[26:33], v[58:65], v[78:81]
	s_setprio 0
	s_barrier
	s_add_i32 s87, s87, 2
	s_add_u32 s38, s38, 0x100
	s_addc_u32 s39, s39, 0
	s_add_u32 s85, s85, 0x100
	s_addc_u32 s86, s86, 0
	s_cmp_gt_u32 s87, 5
	s_cbranch_scc1 .LBB0_992
.LBB0_986:
	ds_read_b128 v[18:21], v220
	ds_read_b128 v[22:25], v220 offset:16
	ds_read_b128 v[26:29], v220 offset:2048
	ds_read_b128 v[30:33], v220 offset:2064
	ds_read_b128 v[2:5], v221
	ds_read_b128 v[6:9], v221 offset:16
	ds_read_b128 v[10:13], v221 offset:2048
	ds_read_b128 v[14:17], v221 offset:2064
	s_cmp_eq_u32 s87, 4
	s_cselect_b64 s[44:45], -1, 0
	v_lshl_add_u64 v[240:241], s[100:101], 0, v[194:195]
	s_add_i32 m0, s35, 0x1c000
	s_nop 0
	global_load_lds_dwordx4 v[240:241], off
	v_lshl_add_u64 v[240:241], s[100:101], 0, v[196:197]
	s_add_i32 m0, s35, 0x1e000
	s_nop 0
	global_load_lds_dwordx4 v[240:241], off
	s_add_i32 m0, s35, 0xc000
	ds_read_b128 v[58:61], v222
	ds_read_b128 v[62:65], v222 offset:16
	ds_read_b128 v[50:53], v222 offset:2048
	ds_read_b128 v[54:57], v222 offset:2064
	ds_read_b128 v[42:45], v222 offset:4096
	ds_read_b128 v[46:49], v222 offset:4112
	ds_read_b128 v[34:37], v222 offset:6144
	ds_read_b128 v[38:41], v222 offset:6160
	global_load_lds_dwordx4 v215, s[38:39]
	s_add_i32 m0, s35, 0xe000
	s_and_b64 s[46:47], s[36:37], s[44:45]
	global_load_lds_dwordx4 v216, s[38:39]
	s_andn2_b64 vcc, exec, s[46:47]
	s_cbranch_vccnz .LBB0_988
	v_mov_b32_e32 v198, v1
	s_nop 0
	v_ashrrev_i32_e32 v201, 31, v198
	v_lshrrev_b32_e32 v201, 26, v201
	v_lshlrev_b32_e32 v200, 4, v198
	v_add_u32_e32 v201, v198, v201
	v_bfe_i32 v198, v198, 27, 1
	v_lshrrev_b32_e32 v198, 22, v198
	v_add_u32_e32 v198, v200, v198
	v_and_b32_e32 v198, 0xfffffc00, v198
	v_sub_u32_e32 v198, v200, v198
	v_lshrrev_b32_e32 v206, 4, v198
	v_bitop3_b32 v198, v206, v198, 32 bitop3:0x6c
	v_ashrrev_i32_e32 v207, 31, v198
	v_ashrrev_i32_e32 v201, 6, v201
	v_lshrrev_b32_e32 v207, 26, v207
	v_lshlrev_b32_e32 v206, 3, v201
	v_add_u32_e32 v207, v198, v207
	v_and_b32_e32 v206, 0x3ffffff0, v206
	v_ashrrev_i32_e32 v208, 6, v207
	v_lshlrev_b32_e32 v201, 5, v201
	v_add_u32_e32 v206, v208, v206
	v_and_b32_e32 v208, 32, v201
	v_and_b32_e32 v201, 0xc0, v207
	v_add_u32_e32 v200, 0x2000, v200
	v_sub_u32_e32 v198, v198, v201
	v_ashrrev_i32_e32 v201, 31, v200
	v_lshrrev_b32_e32 v201, 22, v201
	v_add_u32_e32 v201, v200, v201
	v_ashrrev_i32_e32 v201, 10, v201
	v_mul_i32_i24_e32 v207, 0x400, v201
	v_sub_u32_e32 v200, v200, v207
	v_lshrrev_b32_e32 v207, 4, v200
	v_bitop3_b32 v200, v207, v200, 32 bitop3:0x6c
	v_ashrrev_i32_e32 v209, 31, v200
	v_lshrrev_b32_e32 v209, 26, v209
	v_lshlrev_b32_e32 v207, 3, v201
	v_add_u32_e32 v209, v200, v209
	v_and_b32_e32 v207, 0x3ffffff0, v207
	v_ashrrev_i32_e32 v210, 6, v209
	v_lshlrev_b32_e32 v201, 5, v201
	v_add_u32_e32 v207, v210, v207
	v_and_b32_e32 v210, 32, v201
	v_and_b32_e32 v201, 0xc0, v209
	v_sub_u32_e32 v200, v200, v201
	v_ashrrev_i16_sdwa v209, v214, sext(v200) dst_sel:DWORD dst_unused:UNUSED_PAD src0_sel:DWORD src1_sel:BYTE_0
	v_lshl_add_u32 v200, v206, 2, s82
	v_lshl_add_u32 v206, v207, 2, s82
	ds_read2st64_b32 v[200:201], v200 offset1:2
	ds_read2st64_b32 v[206:207], v206 offset1:2
	v_ashrrev_i16_sdwa v198, v214, sext(v198) dst_sel:DWORD dst_unused:UNUSED_PAD src0_sel:DWORD src1_sel:BYTE_0
	v_bfe_i32 v198, v198, 0, 16
	v_bfe_i32 v209, v209, 0, 16
	v_add_lshl_u32 v208, v208, v198, 1
	v_add_lshl_u32 v209, v210, v209, 1
	s_waitcnt lgkmcnt(0)
	v_lshl_add_u32 v198, v200, 10, v208
	v_lshl_add_u32 v200, v206, 10, v209
	v_lshl_add_u32 v215, v201, 10, v208
	v_lshl_add_u32 v216, v207, 10, v209

.LBB0_990:
	s_add_u32 s46, s38, 0x80
	s_addc_u32 s47, s39, 0
	s_waitcnt lgkmcnt(0)
	s_and_b64 s[44:45], s[44:45], exec
	s_cselect_b32 s47, s15, s47
	s_cselect_b32 s46, s14, s46
	s_cselect_b32 s45, s2, s86
	s_cselect_b32 s44, s11, s85
	s_barrier
	s_setprio 1
	s_waitcnt lgkmcnt(0)
	v_mfma_f32_16x16x128_f8f6f4 v[190:193], v[18:25], v[58:65], v[190:193]
	v_mfma_f32_16x16x128_f8f6f4 v[186:189], v[26:33], v[58:65], v[186:189]
	v_mfma_f32_16x16x128_f8f6f4 v[174:177], v[18:25], v[50:57], v[174:177]
	v_mfma_f32_16x16x128_f8f6f4 v[170:173], v[26:33], v[50:57], v[170:173]
	v_mfma_f32_16x16x128_f8f6f4 v[158:161], v[18:25], v[42:49], v[158:161]
	v_mfma_f32_16x16x128_f8f6f4 v[154:157], v[26:33], v[42:49], v[154:157]
	v_mfma_f32_16x16x128_f8f6f4 v[142:145], v[18:25], v[34:41], v[142:145]
	v_mfma_f32_16x16x128_f8f6f4 v[138:141], v[26:33], v[34:41], v[138:141]
	s_setprio 0
	s_setprio 1
	v_mfma_f32_16x16x128_f8f6f4 v[182:185], v[2:9], v[58:65], v[182:185]
	v_mfma_f32_16x16x128_f8f6f4 v[178:181], v[10:17], v[58:65], v[178:181]
	v_mfma_f32_16x16x128_f8f6f4 v[166:169], v[2:9], v[50:57], v[166:169]
	v_mfma_f32_16x16x128_f8f6f4 v[162:165], v[10:17], v[50:57], v[162:165]
	v_mfma_f32_16x16x128_f8f6f4 v[150:153], v[2:9], v[42:49], v[150:153]
	v_mfma_f32_16x16x128_f8f6f4 v[146:149], v[10:17], v[42:49], v[146:149]
	v_mfma_f32_16x16x128_f8f6f4 v[134:137], v[2:9], v[34:41], v[134:137]
	v_mfma_f32_16x16x128_f8f6f4 v[130:133], v[10:17], v[34:41], v[130:133]
	s_setprio 0
	s_barrier
	s_mov_b32 m0, s60
	v_lshl_add_u64 v[208:209], s[44:45], 0, v[194:195]
	s_add_u32 s98, s44, 0x20000
	ds_read_b128 v[58:61], v222 offset:16384
	ds_read_b128 v[62:65], v222 offset:16400
	ds_read_b128 v[50:53], v222 offset:18432
	ds_read_b128 v[54:57], v222 offset:18448
	ds_read_b128 v[42:45], v222 offset:20480
	ds_read_b128 v[46:49], v222 offset:20496
	ds_read_b128 v[34:37], v222 offset:22528
	ds_read_b128 v[38:41], v222 offset:22544
	global_load_lds_dwordx4 v[208:209], off
	v_lshl_add_u64 v[206:207], s[44:45], 0, v[196:197]
	s_mov_b32 m0, s61
	s_addc_u32 s99, s45, 0
	global_load_lds_dwordx4 v[206:207], off
	s_mov_b32 m0, s35
	s_nop 0
	global_load_lds_dwordx4 v198, s[46:47]
	s_mov_b32 m0, s64
	s_nop 0
	global_load_lds_dwordx4 v200, s[46:47]
	s_waitcnt vmcnt(6)
	s_branch .LBB0_985

	.amdhsa_kernel _Z6mk_fwd4Args
		.amdhsa_group_segment_fixed_size 0
		.amdhsa_private_segment_fixed_size 0
		.amdhsa_kernarg_size 416
		.amdhsa_user_sgpr_count 2
		.amdhsa_user_sgpr_dispatch_ptr 0
		.amdhsa_user_sgpr_queue_ptr 0
		.amdhsa_user_sgpr_kernarg_segment_ptr 1
		.amdhsa_user_sgpr_dispatch_id 0
		.amdhsa_user_sgpr_kernarg_preload_length 0
		.amdhsa_user_sgpr_kernarg_preload_offset 0
		.amdhsa_user_sgpr_private_segment_size 0
		.amdhsa_uses_dynamic_stack 0
		.amdhsa_enable_private_segment 0
		.amdhsa_system_sgpr_workgroup_id_x 1
		.amdhsa_system_sgpr_workgroup_id_y 0
		.amdhsa_system_sgpr_workgroup_id_z 0
		.amdhsa_system_sgpr_workgroup_info 0
		.amdhsa_system_vgpr_workitem_id 0
		.amdhsa_next_free_vgpr 248
		.amdhsa_next_free_sgpr 102
		.amdhsa_accum_offset 248
		.amdhsa_reserve_vcc 1
		.amdhsa_float_round_mode_32 0
		.amdhsa_float_round_mode_16_64 0
		.amdhsa_float_denorm_mode_32 3
		.amdhsa_float_denorm_mode_16_64 3
		.amdhsa_dx10_clamp 1
		.amdhsa_ieee_mode 1
		.amdhsa_fp16_overflow 0
		.amdhsa_tg_split 0
		.amdhsa_exception_fp_ieee_invalid_op 0
		.amdhsa_exception_fp_denorm_src 0
		.amdhsa_exception_fp_ieee_div_zero 0
		.amdhsa_exception_fp_ieee_overflow 0
		.amdhsa_exception_fp_ieee_underflow 0
		.amdhsa_exception_fp_ieee_inexact 0
		.amdhsa_exception_int_div_zero 0
	.end_amdhsa_kernel

amdhsa.kernels:
  - .agpr_count:     0
    .args:
      - .offset:         0
        .size:           160
        .value_kind:     by_value
      - .offset:         160
        .size:           4
        .value_kind:     hidden_block_count_x
      - .offset:         164
        .size:           4
        .value_kind:     hidden_block_count_y
      - .offset:         168
        .size:           4
        .value_kind:     hidden_block_count_z
      - .offset:         172
        .size:           2
        .value_kind:     hidden_group_size_x
      - .offset:         174
        .size:           2
        .value_kind:     hidden_group_size_y
      - .offset:         176
        .size:           2
        .value_kind:     hidden_group_size_z
      - .offset:         178
        .size:           2
        .value_kind:     hidden_remainder_x
      - .offset:         180
        .size:           2
        .value_kind:     hidden_remainder_y
      - .offset:         182
        .size:           2
        .value_kind:     hidden_remainder_z
      - .offset:         200
        .size:           8
        .value_kind:     hidden_global_offset_x
      - .offset:         208
        .size:           8
        .value_kind:     hidden_global_offset_y
      - .offset:         216
        .size:           8
        .value_kind:     hidden_global_offset_z
      - .offset:         224
        .size:           2
        .value_kind:     hidden_grid_dims
      - .offset:         280
        .size:           4
        .value_kind:     hidden_dynamic_lds_size
    .group_segment_fixed_size: 0
    .kernarg_segment_align: 8
    .kernarg_segment_size: 416
    .language:       OpenCL C
    .language_version:
      - 2
      - 0
    .max_flat_workgroup_size: 512
    .name:           _Z6mk_fwd4Args
    .private_segment_fixed_size: 0
    .sgpr_count:     108
    .sgpr_spill_count: 115
    .symbol:         _Z6mk_fwd4Args.kd
    .uniform_work_group_size: 1
    .uses_dynamic_stack: false
    .vgpr_count:     248
    .vgpr_spill_count: 0
    .wavefront_size: 64
